# speedup vs baseline: 1.0142x; 1.0124x over previous
_Z16bilateral_kernelPKfS0_Pf:
	s_load_dwordx2 s[4:5], s[0:1], 0x0
	s_load_dwordx2 s[8:9], s[0:1], 0x10
	s_lshr_b32 s19, s2, 8
	s_and_b32 s0, s2, 7
	s_mulk_i32 s0, 0x60
	s_lshr_b32 s1, s2, 3
	s_add_i32 s1, s0, s1
	s_lshr_b32 s0, s1, 6
	s_lshl_b32 s11, s1, 6
	s_nop 0
	s_and_b32 s11, s11, 0x1c0
	s_lshl_b32 s1, s1, 3
	s_nop 0
	s_and_b32 s10, s1, 0x1c0
	s_mov_b32 s1, 0
	s_lshl_b64 s[2:3], s[0:1], 20
	s_mov_b32 s20, 0xc05dfbe6
	s_mov_b32 s21, 0xc05dfbe6
	s_mov_b32 s22, 0xc0a8390e
	s_mov_b32 s23, 0xc0a8390e
	s_mov_b32 s24, 0xc08211a7
	s_mov_b32 s25, 0xc08211a7
	s_mov_b32 s26, 0xc0bb4cc1
	s_mov_b32 s27, 0xc0bb4cc1
	s_mov_b32 s28, 0xc0f487dc
	s_mov_b32 s29, 0xc0f487dc
	s_mov_b32 s30, 0x3e0bd796
	s_mov_b32 s31, 0x3e0bd796
	s_mov_b32 s32, 0x3f45a90c
	s_mov_b32 s33, 0x3f45a90c
	s_mov_b32 s34, 0x3fa5c782
	s_mov_b32 s35, 0x3fa5c782
	v_and_b32_e32 v118, 15, v0
	v_lshrrev_b32_e32 v115, 2, v0
	v_lshl_or_b32 v113, v118, 2, s11
	v_and_or_b32 v117, v115, 60, s10
	v_min_u32_e32 v116, 0x1fa, v113
	v_sub_u32_e64 v115, v113, 2 clamp
	v_add_u32_e64 v116, 4, v116
	v_cmp_eq_u32_e64 s[16:17], 0, v118
	v_cmp_eq_u32_e32 vcc, 15, v118
	s_nop 1
	v_cndmask_b32_e64 v115, v116, v115, s[16:17]
	s_or_b64 vcc, s[16:17], vcc
	v_lshlrev_b32_e32 v115, 2, v115
	v_mov_b32_e32 v116, 0x7ff00000
	s_nop 0
	v_cndmask_b32_e32 v112, v116, v115, vcc
	s_movk_i32 s18, 0x1fc
	v_cmp_eq_u32_e32 vcc, 0, v113
	v_cmp_eq_u32_e64 s[16:17], s18, v113
	v_lshlrev_b32_e32 v113, 2, v113
	s_waitcnt lgkmcnt(0)
	s_add_u32 s4, s4, s2
	s_addc_u32 s5, s5, s3
	s_and_b32 s5, s5, 0xffff
	s_mov_b32 s6, 0x100000
	s_mov_b32 s7, 0x20000
	s_add_u32 s12, s8, s2
	s_addc_u32 s13, s9, s3
	s_and_b32 s13, s13, 0xffff
	s_mov_b32 s14, 0x100000
	s_mov_b32 s15, 0x20000
	s_cmp_eq_u32 s19, 0
	s_cbranch_scc1 .Lmynosl
	s_sleep 4
	s_cmp_eq_u32 s19, 1
	s_cbranch_scc1 .Lmynosl
	s_sleep 4
.Lmynosl:
	v_sub_u32_e64 v115, v117, 2 clamp
	v_lshlrev_b32_e32 v115, 11, v115
	v_add_u32_e32 v116, v115, v112
	v_add_u32_e64 v115, v115, v113
	buffer_load_dwordx2 v[0:1], v116, s[4:7], 0 offen nt
	buffer_load_dwordx2 v[6:7], v116, s[4:7], 0 offen nt
	buffer_load_dwordx4 v[2:5], v115, s[4:7], 0 offen nt
	v_sub_u32_e64 v115, v117, 1 clamp
	v_lshlrev_b32_e32 v115, 11, v115
	v_add_u32_e32 v116, v115, v112
	v_add_u32_e64 v115, v115, v113
	buffer_load_dwordx2 v[8:9], v116, s[4:7], 0 offen nt
	buffer_load_dwordx2 v[14:15], v116, s[4:7], 0 offen nt
	buffer_load_dwordx4 v[10:13], v115, s[4:7], 0 offen nt
	v_lshlrev_b32_e32 v115, 11, v117
	v_add_u32_e32 v116, v115, v112
	v_add_u32_e64 v114, v115, v113
	v_add_u32_e32 v119, 0x1000, v114
	buffer_load_dwordx2 v[16:17], v116, s[4:7], 0 offen nt
	buffer_load_dwordx2 v[22:23], v116, s[4:7], 0 offen nt
	buffer_load_dwordx4 v[18:21], v114, s[4:7], 0 offen nt
	v_lshlrev_b32_e64 v115, 11, v117
	v_add_u32_e32 v115, 0x800, v115
	v_add_u32_e32 v116, v115, v112
	v_add_u32_e32 v115, v115, v113
	buffer_load_dwordx2 v[24:25], v116, s[4:7], 0 offen nt
	buffer_load_dwordx2 v[30:31], v116, s[4:7], 0 offen nt
	buffer_load_dwordx4 v[26:29], v115, s[4:7], 0 offen nt
	v_lshlrev_b32_e64 v115, 11, v117
	v_add_u32_e32 v115, 0x1000, v115
	v_add_u32_e32 v116, v115, v112
	v_add_u32_e32 v115, v115, v113
	buffer_load_dwordx2 v[32:33], v116, s[4:7], 0 offen nt
	buffer_load_dwordx2 v[38:39], v116, s[4:7], 0 offen nt
	buffer_load_dwordx4 v[34:37], v115, s[4:7], 0 offen nt
	v_lshlrev_b32_e64 v115, 11, v117
	v_add_u32_e32 v115, 0x1800, v115
	v_add_u32_e32 v116, v115, v112
	v_add_u32_e32 v115, v115, v113
	buffer_load_dwordx2 v[40:41], v116, s[4:7], 0 offen nt
	buffer_load_dwordx2 v[46:47], v116, s[4:7], 0 offen nt
	buffer_load_dwordx4 v[42:45], v115, s[4:7], 0 offen nt
	v_min_u32_e32 v115, 0x1fb, v117
	v_lshlrev_b32_e64 v115, 11, v115
	v_add_u32_e32 v115, 0x2000, v115
	v_add_u32_e32 v116, v115, v112
	v_add_u32_e32 v115, v115, v113
	buffer_load_dwordx2 v[48:49], v116, s[4:7], 0 offen nt
	buffer_load_dwordx2 v[54:55], v116, s[4:7], 0 offen nt
	buffer_load_dwordx4 v[50:53], v115, s[4:7], 0 offen nt
	v_min_u32_e32 v115, 0x1fa, v117
	v_lshlrev_b32_e64 v115, 11, v115
	v_add_u32_e32 v115, 0x2800, v115
	v_add_u32_e32 v116, v115, v112
	v_add_u32_e32 v115, v115, v113
	buffer_load_dwordx2 v[56:57], v116, s[4:7], 0 offen nt
	buffer_load_dwordx2 v[62:63], v116, s[4:7], 0 offen nt
	buffer_load_dwordx4 v[58:61], v115, s[4:7], 0 offen nt
	s_cmp_eq_u32 s19, 0
	s_cbranch_scc1 .Lmyp0
	s_cmp_eq_u32 s19, 1
	s_cbranch_scc1 .Lmyp1
	s_setprio 0
	s_branch .Lmypd
